# baseline (speedup 1.0000x reference)
_Z11edge_kernelILi36ELb1EEvPKfS1_PKDF16_PKiS5_S1_S1_S1_S1_S1_PDF16_:
	s_load_dwordx8 s[4:11], s[0:1], 0x0
	s_load_dwordx8 s[12:19], s[0:1], 0x20
	s_load_dwordx4 s[20:23], s[0:1], 0x40
	s_load_dwordx2 s[24:25], s[0:1], 0x50
	v_readfirstlane_b32 s3, v0
	v_bfe_u32 v139, v0, 4, 2
	v_and_b32_e32 v140, 15, v0
	v_and_b32_e32 v142, 63, v0
	s_lshr_b32 s3, s3, 6
	s_lshl_b32 s2, s2, 1
	s_add_i32 s2, s2, s3
	v_lshlrev_b32_e32 v138, 12, v139
	v_lshl_or_b32 v138, v140, 4, v138
	v_lshlrev_b32_e32 v143, 4, v142
	v_lshl_or_b32 v141, v140, 2, v139
	v_lshlrev_b32_e32 v141, 2, v141
	v_mul_u32_u24_e32 v137, 0x900, v139
	v_lshl_or_b32 v137, v140, 4, v137
	v_mul_u32_u24_e32 v142, 36, v139
	s_mul_i32 s28, s2, 0x2400
	s_lshl_b32 s29, s2, 14
	s_lshl_b32 s30, s2, 2
	s_lshl_b32 s31, s2, 8
	s_lshl_b32 s33, s3, 10
	s_lshl_b32 s34, s3, 8
	s_addk_i32 s34, 0x4000
	s_waitcnt lgkmcnt(0)
	s_add_u32 s10, s10, s30
	s_addc_u32 s11, s11, 0
	s_add_u32 s12, s12, s30
	s_addc_u32 s13, s13, 0
	s_load_dword s35, s[10:11], 0x0
	s_load_dword s36, s[12:13], 0x0
	s_add_u32 s14, s14, s28
	s_addc_u32 s15, s15, 0
	global_load_dwordx4 v[0:3], v137, s[14:15] nt
	global_load_dwordx4 v[4:7], v137, s[14:15] offset:256 nt
	global_load_dwordx4 v[8:11], v137, s[14:15] offset:512 nt
	global_load_dwordx4 v[12:15], v137, s[14:15] offset:768 nt
	global_load_dwordx4 v[16:19], v137, s[14:15] offset:1024 nt
	global_load_dwordx4 v[20:23], v137, s[14:15] offset:1280 nt
	global_load_dwordx4 v[24:27], v137, s[14:15] offset:1536 nt
	global_load_dwordx4 v[28:31], v137, s[14:15] offset:1792 nt
	global_load_dwordx4 v[32:35], v137, s[14:15] offset:2048 nt
	s_add_u32 s22, s22, s33
	s_addc_u32 s23, s23, 0
	s_mov_b32 m0, s33
	s_add_u32 s18, s18, s29
	s_addc_u32 s19, s19, 0
	global_load_lds_dwordx4 v143, s[22:23]
	global_load_lds_dwordx4 v143, s[22:23] offset:2048
	s_add_u32 m0, m0, 0x1000
	s_add_u32 s22, s22, 0x1000
	s_addc_u32 s23, s23, 0
	global_load_lds_dwordx4 v143, s[22:23]
	global_load_lds_dwordx4 v143, s[22:23] offset:2048
	s_add_u32 m0, m0, 0x1000
	s_add_u32 s22, s22, 0x1000
	s_addc_u32 s23, s23, 0
	global_load_lds_dwordx4 v143, s[22:23]
	global_load_lds_dwordx4 v143, s[22:23] offset:2048
	s_add_u32 m0, m0, 0x1000
	s_add_u32 s22, s22, 0x1000
	s_addc_u32 s23, s23, 0
	global_load_lds_dwordx4 v143, s[22:23]
	global_load_lds_dwordx4 v143, s[22:23] offset:2048
	s_add_u32 s16, s16, s31
	s_addc_u32 s17, s17, 0
	s_add_u32 s20, s20, s31
	s_addc_u32 s21, s21, 0
	s_waitcnt lgkmcnt(0)
	s_lshl_b32 s36, s36, 7
	s_add_u32 s24, s24, s36
	s_addc_u32 s25, s25, 0
	s_lshl_b32 s37, s35, 7
	s_lshl_b32 s38, s35, 4
	s_add_u32 s4, s4, s37
	s_addc_u32 s5, s5, 0
	s_add_u32 s6, s6, s38
	s_addc_u32 s7, s7, 0
	v_mov_b32_e32 v157, 0
	v_mov_b32_e32 v156, v142
	v_lshl_add_u64 v[158:159], s[4:5], 0, v[156:157]
	v_lshl_add_u64 v[158:159], v[158:159], 0, 20
	v_cmp_eq_u32_e32 vcc, 3, v139
	s_nop 1
	v_mov_b32_e32 v154, s6
	v_mov_b32_e32 v155, s7
	v_cndmask_b32_e32 v158, v158, v154, vcc
	v_cndmask_b32_e32 v159, v159, v155, vcc
	global_load_dwordx4 v[144:147], v142, s[4:5] nt
	global_load_dword v148, v142, s[4:5] offset:16 nt
	global_load_dwordx4 v[150:153], v[158:159], off nt
	global_load_dword v136, v141, s[16:17] nt
	global_load_dword v128, v141, s[20:21] nt
	global_load_dwordx4 v[64:67], v138, s[18:19] nt
	global_load_dwordx4 v[68:71], v138, s[18:19] offset:256 nt
	global_load_dwordx4 v[72:75], v138, s[18:19] offset:512 nt
	global_load_dwordx4 v[76:79], v138, s[18:19] offset:768 nt
	global_load_dwordx4 v[80:83], v138, s[18:19] offset:1024 nt
	global_load_dwordx4 v[84:87], v138, s[18:19] offset:1280 nt
	global_load_dwordx4 v[88:91], v138, s[18:19] offset:1536 nt
	global_load_dwordx4 v[92:95], v138, s[18:19] offset:1792 nt
	global_load_dwordx4 v[96:99], v138, s[18:19] offset:2048 nt
	global_load_dwordx4 v[100:103], v138, s[18:19] offset:2304 nt
	global_load_dwordx4 v[104:107], v138, s[18:19] offset:2560 nt
	global_load_dwordx4 v[108:111], v138, s[18:19] offset:2816 nt
	global_load_dwordx4 v[112:115], v138, s[18:19] offset:3072 nt
	global_load_dwordx4 v[116:119], v138, s[18:19] offset:3328 nt
	global_load_dwordx4 v[120:123], v138, s[18:19] offset:3584 nt
	global_load_dwordx4 v[124:127], v138, s[18:19] offset:3840 nt
	v_add_u32_e32 v142, s34, v141
	v_lshl_add_u32 v143, v139, 6, s34
	s_waitcnt vmcnt(18)
	s_barrier
	v_pk_mul_f32 v[160:161], v[144:145], v[0:1] op_sel_hi:[0,1]
	v_pk_mul_f32 v[162:163], v[144:145], v[2:3] op_sel_hi:[0,1]
	v_pk_mul_f32 v[164:165], v[144:145], v[4:5] op_sel:[1,0]
	v_pk_mul_f32 v[166:167], v[144:145], v[6:7] op_sel:[1,0]
	v_pk_fma_f32 v[160:161], v[146:147], v[8:9], v[160:161] op_sel_hi:[0,1,1]
	v_pk_fma_f32 v[162:163], v[146:147], v[10:11], v[162:163] op_sel_hi:[0,1,1]
	v_pk_fma_f32 v[164:165], v[146:147], v[12:13], v[164:165] op_sel:[1,0,0]
	v_pk_fma_f32 v[166:167], v[146:147], v[14:15], v[166:167] op_sel:[1,0,0]
	v_pk_fma_f32 v[160:161], v[148:149], v[16:17], v[160:161] op_sel_hi:[0,1,1]
	v_pk_fma_f32 v[162:163], v[148:149], v[18:19], v[162:163] op_sel_hi:[0,1,1]
	v_pk_fma_f32 v[164:165], v[150:151], v[20:21], v[164:165] op_sel_hi:[0,1,1]
	v_pk_fma_f32 v[166:167], v[150:151], v[22:23], v[166:167] op_sel_hi:[0,1,1]
	v_pk_fma_f32 v[160:161], v[150:151], v[24:25], v[160:161] op_sel:[1,0,0]
	v_pk_fma_f32 v[162:163], v[150:151], v[26:27], v[162:163] op_sel:[1,0,0]
	v_pk_fma_f32 v[164:165], v[152:153], v[28:29], v[164:165] op_sel_hi:[0,1,1]
	v_pk_fma_f32 v[166:167], v[152:153], v[30:31], v[166:167] op_sel_hi:[0,1,1]
	v_pk_fma_f32 v[160:161], v[152:153], v[32:33], v[160:161] op_sel:[1,0,0]
	v_pk_fma_f32 v[162:163], v[152:153], v[34:35], v[162:163] op_sel:[1,0,0]
	v_pk_add_f32 v[160:161], v[160:161], v[164:165]
	v_pk_add_f32 v[162:163], v[162:163], v[166:167]
	s_nop 1
	v_permlane16_swap_b32_e32 v160, v161
	v_permlane16_swap_b32_e32 v162, v163
	v_add_f32_e32 v160, v160, v161
	v_add_f32_e32 v162, v162, v163
	s_nop 1
	v_permlane32_swap_b32_e32 v160, v162
	v_add_f32_e32 v160, v160, v162
	s_waitcnt vmcnt(17)
	v_add_f32_e32 v160, v160, v136
	v_max_f32_e32 v160, 0, v160
	ds_write_b32 v142, v160
	ds_read_b128 v[144:147], v143
	ds_read_b128 v[148:151], v143 offset:16
	ds_read_b128 v[152:155], v143 offset:32
	ds_read_b128 v[156:159], v143 offset:48
	ds_read_b128 v[0:3], v138
	ds_read_b128 v[4:7], v138 offset:256
	ds_read_b128 v[8:11], v138 offset:512
	ds_read_b128 v[12:15], v138 offset:768
	ds_read_b128 v[16:19], v138 offset:1024
	ds_read_b128 v[20:23], v138 offset:1280
	ds_read_b128 v[24:27], v138 offset:1536
	ds_read_b128 v[28:31], v138 offset:1792
	s_waitcnt lgkmcnt(8)
	s_waitcnt vmcnt(12)
	v_pk_mul_f32 v[160:161], v[144:145], v[64:65] op_sel_hi:[0,1]
	v_pk_mul_f32 v[162:163], v[144:145], v[66:67] op_sel_hi:[0,1]
	v_pk_mul_f32 v[164:165], v[144:145], v[68:69] op_sel:[1,0]
	v_pk_mul_f32 v[166:167], v[144:145], v[70:71] op_sel:[1,0]
	v_pk_fma_f32 v[160:161], v[146:147], v[72:73], v[160:161] op_sel_hi:[0,1,1]
	v_pk_fma_f32 v[162:163], v[146:147], v[74:75], v[162:163] op_sel_hi:[0,1,1]
	v_pk_fma_f32 v[164:165], v[146:147], v[76:77], v[164:165] op_sel:[1,0,0]
	v_pk_fma_f32 v[166:167], v[146:147], v[78:79], v[166:167] op_sel:[1,0,0]
	ds_read_b128 v[32:35], v138 offset:2048
	ds_read_b128 v[36:39], v138 offset:2304
	ds_read_b128 v[40:43], v138 offset:2560
	ds_read_b128 v[44:47], v138 offset:2816
	s_waitcnt vmcnt(8)
	v_pk_fma_f32 v[160:161], v[148:149], v[80:81], v[160:161] op_sel_hi:[0,1,1]
	v_pk_fma_f32 v[162:163], v[148:149], v[82:83], v[162:163] op_sel_hi:[0,1,1]
	v_pk_fma_f32 v[164:165], v[148:149], v[84:85], v[164:165] op_sel:[1,0,0]
	v_pk_fma_f32 v[166:167], v[148:149], v[86:87], v[166:167] op_sel:[1,0,0]
	v_pk_fma_f32 v[160:161], v[150:151], v[88:89], v[160:161] op_sel_hi:[0,1,1]
	v_pk_fma_f32 v[162:163], v[150:151], v[90:91], v[162:163] op_sel_hi:[0,1,1]
	v_pk_fma_f32 v[164:165], v[150:151], v[92:93], v[164:165] op_sel:[1,0,0]
	v_pk_fma_f32 v[166:167], v[150:151], v[94:95], v[166:167] op_sel:[1,0,0]
	s_waitcnt lgkmcnt(4)
	ds_read_b128 v[48:51], v138 offset:3072
	ds_read_b128 v[52:55], v138 offset:3328
	ds_read_b128 v[56:59], v138 offset:3584
	ds_read_b128 v[60:63], v138 offset:3840
	s_waitcnt vmcnt(4)
	v_pk_fma_f32 v[160:161], v[152:153], v[96:97], v[160:161] op_sel_hi:[0,1,1]
	v_pk_fma_f32 v[162:163], v[152:153], v[98:99], v[162:163] op_sel_hi:[0,1,1]
	v_pk_fma_f32 v[164:165], v[152:153], v[100:101], v[164:165] op_sel:[1,0,0]
	v_pk_fma_f32 v[166:167], v[152:153], v[102:103], v[166:167] op_sel:[1,0,0]
	v_pk_fma_f32 v[160:161], v[154:155], v[104:105], v[160:161] op_sel_hi:[0,1,1]
	v_pk_fma_f32 v[162:163], v[154:155], v[106:107], v[162:163] op_sel_hi:[0,1,1]
	v_pk_fma_f32 v[164:165], v[154:155], v[108:109], v[164:165] op_sel:[1,0,0]
	v_pk_fma_f32 v[166:167], v[154:155], v[110:111], v[166:167] op_sel:[1,0,0]
	s_waitcnt vmcnt(0)
	v_pk_fma_f32 v[160:161], v[156:157], v[112:113], v[160:161] op_sel_hi:[0,1,1]
	v_pk_fma_f32 v[162:163], v[156:157], v[114:115], v[162:163] op_sel_hi:[0,1,1]
	v_pk_fma_f32 v[164:165], v[156:157], v[116:117], v[164:165] op_sel:[1,0,0]
	v_pk_fma_f32 v[166:167], v[156:157], v[118:119], v[166:167] op_sel:[1,0,0]
	v_pk_fma_f32 v[160:161], v[158:159], v[120:121], v[160:161] op_sel_hi:[0,1,1]
	v_pk_fma_f32 v[162:163], v[158:159], v[122:123], v[162:163] op_sel_hi:[0,1,1]
	v_pk_fma_f32 v[164:165], v[158:159], v[124:125], v[164:165] op_sel:[1,0,0]
	v_pk_fma_f32 v[166:167], v[158:159], v[126:127], v[166:167] op_sel:[1,0,0]
	v_pk_add_f32 v[160:161], v[160:161], v[164:165]
	v_pk_add_f32 v[162:163], v[162:163], v[166:167]
	s_nop 1
	v_permlane16_swap_b32_e32 v160, v161
	v_permlane16_swap_b32_e32 v162, v163
	v_add_f32_e32 v160, v160, v161
	v_add_f32_e32 v162, v162, v163
	s_nop 1
	v_permlane32_swap_b32_e32 v160, v162
	v_add_f32_e32 v160, v160, v162
	v_add_f32_e32 v160, v160, v128
	ds_write_b32 v142, v160
	ds_read_b128 v[144:147], v143
	ds_read_b128 v[148:151], v143 offset:16
	ds_read_b128 v[152:155], v143 offset:32
	ds_read_b128 v[156:159], v143 offset:48
	v_lshlrev_b32_e32 v136, 3, v140
	v_lshl_or_b32 v136, v139, 2, v136
	v_cmp_gt_u32_e32 vcc, 2, v139
	s_waitcnt lgkmcnt(0)
	v_pk_mul_f32 v[160:161], v[144:145], v[0:1] op_sel_hi:[0,1]
	v_pk_mul_f32 v[162:163], v[144:145], v[2:3] op_sel_hi:[0,1]
	v_pk_mul_f32 v[164:165], v[144:145], v[4:5] op_sel:[1,0]
	v_pk_mul_f32 v[166:167], v[144:145], v[6:7] op_sel:[1,0]
	v_pk_fma_f32 v[160:161], v[146:147], v[8:9], v[160:161] op_sel_hi:[0,1,1]
	v_pk_fma_f32 v[162:163], v[146:147], v[10:11], v[162:163] op_sel_hi:[0,1,1]
	v_pk_fma_f32 v[164:165], v[146:147], v[12:13], v[164:165] op_sel:[1,0,0]
	v_pk_fma_f32 v[166:167], v[146:147], v[14:15], v[166:167] op_sel:[1,0,0]
	v_pk_fma_f32 v[160:161], v[148:149], v[16:17], v[160:161] op_sel_hi:[0,1,1]
	v_pk_fma_f32 v[162:163], v[148:149], v[18:19], v[162:163] op_sel_hi:[0,1,1]
	v_pk_fma_f32 v[164:165], v[148:149], v[20:21], v[164:165] op_sel:[1,0,0]
	v_pk_fma_f32 v[166:167], v[148:149], v[22:23], v[166:167] op_sel:[1,0,0]
	v_pk_fma_f32 v[160:161], v[150:151], v[24:25], v[160:161] op_sel_hi:[0,1,1]
	v_pk_fma_f32 v[162:163], v[150:151], v[26:27], v[162:163] op_sel_hi:[0,1,1]
	v_pk_fma_f32 v[164:165], v[150:151], v[28:29], v[164:165] op_sel:[1,0,0]
	v_pk_fma_f32 v[166:167], v[150:151], v[30:31], v[166:167] op_sel:[1,0,0]
	v_pk_fma_f32 v[160:161], v[152:153], v[32:33], v[160:161] op_sel_hi:[0,1,1]
	v_pk_fma_f32 v[162:163], v[152:153], v[34:35], v[162:163] op_sel_hi:[0,1,1]
	v_pk_fma_f32 v[164:165], v[152:153], v[36:37], v[164:165] op_sel:[1,0,0]
	v_pk_fma_f32 v[166:167], v[152:153], v[38:39], v[166:167] op_sel:[1,0,0]
	v_pk_fma_f32 v[160:161], v[154:155], v[40:41], v[160:161] op_sel_hi:[0,1,1]
	v_pk_fma_f32 v[162:163], v[154:155], v[42:43], v[162:163] op_sel_hi:[0,1,1]
	v_pk_fma_f32 v[164:165], v[154:155], v[44:45], v[164:165] op_sel:[1,0,0]
	v_pk_fma_f32 v[166:167], v[154:155], v[46:47], v[166:167] op_sel:[1,0,0]
	v_pk_fma_f32 v[160:161], v[156:157], v[48:49], v[160:161] op_sel_hi:[0,1,1]
	v_pk_fma_f32 v[162:163], v[156:157], v[50:51], v[162:163] op_sel_hi:[0,1,1]
	v_pk_fma_f32 v[164:165], v[156:157], v[52:53], v[164:165] op_sel:[1,0,0]
	v_pk_fma_f32 v[166:167], v[156:157], v[54:55], v[166:167] op_sel:[1,0,0]
	v_pk_fma_f32 v[160:161], v[158:159], v[56:57], v[160:161] op_sel_hi:[0,1,1]
	v_pk_fma_f32 v[162:163], v[158:159], v[58:59], v[162:163] op_sel_hi:[0,1,1]
	v_pk_fma_f32 v[164:165], v[158:159], v[60:61], v[164:165] op_sel:[1,0,0]
	v_pk_fma_f32 v[166:167], v[158:159], v[62:63], v[166:167] op_sel:[1,0,0]
	v_pk_add_f32 v[160:161], v[160:161], v[164:165]
	v_pk_add_f32 v[162:163], v[162:163], v[166:167]
	s_nop 1
	v_permlane16_swap_b32_e32 v160, v162
	v_permlane16_swap_b32_e32 v161, v163
	v_add_f32_e32 v160, v160, v162
	v_add_f32_e32 v161, v161, v163
	v_mov_b32_e32 v144, v160
	v_mov_b32_e32 v145, v161
	s_nop 1
	v_permlane32_swap_b32_e32 v160, v144
	v_permlane32_swap_b32_e32 v161, v145
	v_add_f32_e32 v160, v160, v144
	v_add_f32_e32 v161, v161, v145
	v_cvt_pk_f16_f32 v137, v160, v161
	s_and_saveexec_b64 s[4:5], vcc
	global_atomic_pk_add_f16 v136, v137, s[24:25]
	s_endpgm
	.p2align	8

	.amdhsa_kernel _Z11edge_kernelILi36ELb1EEvPKfS1_PKDF16_PKiS5_S1_S1_S1_S1_S1_PDF16_
		.amdhsa_group_segment_fixed_size 16896
		.amdhsa_private_segment_fixed_size 0
		.amdhsa_kernarg_size 88
		.amdhsa_user_sgpr_count 2
		.amdhsa_user_sgpr_dispatch_ptr 0
		.amdhsa_user_sgpr_queue_ptr 0
		.amdhsa_user_sgpr_kernarg_segment_ptr 1
		.amdhsa_user_sgpr_dispatch_id 0
		.amdhsa_user_sgpr_kernarg_preload_length 0
		.amdhsa_user_sgpr_kernarg_preload_offset 0
		.amdhsa_user_sgpr_private_segment_size 0
		.amdhsa_uses_dynamic_stack 0
		.amdhsa_enable_private_segment 0
		.amdhsa_system_sgpr_workgroup_id_x 1
		.amdhsa_system_sgpr_workgroup_id_y 0
		.amdhsa_system_sgpr_workgroup_id_z 0
		.amdhsa_system_sgpr_workgroup_info 0
		.amdhsa_system_vgpr_workitem_id 0
		.amdhsa_next_free_vgpr 168
		.amdhsa_next_free_sgpr 96
		.amdhsa_accum_offset 168
		.amdhsa_reserve_vcc 1
		.amdhsa_float_round_mode_32 0
		.amdhsa_float_round_mode_16_64 0
		.amdhsa_float_denorm_mode_32 3
		.amdhsa_float_denorm_mode_16_64 3
		.amdhsa_dx10_clamp 1
		.amdhsa_ieee_mode 1
		.amdhsa_fp16_overflow 0
		.amdhsa_tg_split 0
		.amdhsa_exception_fp_ieee_invalid_op 0
		.amdhsa_exception_fp_denorm_src 0
		.amdhsa_exception_fp_ieee_div_zero 0
		.amdhsa_exception_fp_ieee_overflow 0
		.amdhsa_exception_fp_ieee_underflow 0
		.amdhsa_exception_fp_ieee_inexact 0
		.amdhsa_exception_int_div_zero 0
	.end_amdhsa_kernel

_Z11edge_kernelILi64ELb0EEvPKfS1_PKDF16_PKiS5_S1_S1_S1_S1_S1_PDF16_:
	s_load_dwordx16 s[4:19], s[0:1], 0x10
	s_load_dwordx2 s[20:21], s[0:1], 0x50
	v_readfirstlane_b32 s3, v0
	v_bfe_u32 v139, v0, 4, 2
	v_and_b32_e32 v140, 15, v0
	v_and_b32_e32 v142, 63, v0
	s_lshr_b32 s3, s3, 6
	s_lshl_b32 s2, s2, 1
	s_add_i32 s2, s2, s3
	v_lshlrev_b32_e32 v138, 12, v139
	v_lshl_or_b32 v138, v140, 4, v138
	v_lshlrev_b32_e32 v143, 4, v142
	v_lshl_or_b32 v141, v140, 2, v139
	v_lshlrev_b32_e32 v141, 2, v141
	v_lshlrev_b32_e32 v142, 5, v139
	s_lshl_b32 s28, s2, 14
	s_lshl_b32 s29, s2, 14
	s_lshl_b32 s30, s2, 2
	s_lshl_b32 s31, s2, 8
	s_lshl_b32 s33, s3, 10
	s_lshl_b32 s34, s3, 8
	s_addk_i32 s34, 0x4000
	s_waitcnt lgkmcnt(0)
	s_add_u32 s6, s6, s30
	s_addc_u32 s7, s7, 0
	s_add_u32 s8, s8, s30
	s_addc_u32 s9, s9, 0
	s_load_dword s35, s[6:7], 0x0
	s_load_dword s36, s[8:9], 0x0
	s_add_u32 s10, s10, s28
	s_addc_u32 s11, s11, 0
	global_load_dwordx4 v[0:3], v138, s[10:11] nt
	global_load_dwordx4 v[4:7], v138, s[10:11] offset:256 nt
	global_load_dwordx4 v[8:11], v138, s[10:11] offset:512 nt
	global_load_dwordx4 v[12:15], v138, s[10:11] offset:768 nt
	global_load_dwordx4 v[16:19], v138, s[10:11] offset:1024 nt
	global_load_dwordx4 v[20:23], v138, s[10:11] offset:1280 nt
	global_load_dwordx4 v[24:27], v138, s[10:11] offset:1536 nt
	global_load_dwordx4 v[28:31], v138, s[10:11] offset:1792 nt
	global_load_dwordx4 v[32:35], v138, s[10:11] offset:2048 nt
	global_load_dwordx4 v[36:39], v138, s[10:11] offset:2304 nt
	global_load_dwordx4 v[40:43], v138, s[10:11] offset:2560 nt
	global_load_dwordx4 v[44:47], v138, s[10:11] offset:2816 nt
	global_load_dwordx4 v[48:51], v138, s[10:11] offset:3072 nt
	global_load_dwordx4 v[52:55], v138, s[10:11] offset:3328 nt
	global_load_dwordx4 v[56:59], v138, s[10:11] offset:3584 nt
	global_load_dwordx4 v[60:63], v138, s[10:11] offset:3840 nt
	s_add_u32 s18, s18, s33
	s_addc_u32 s19, s19, 0
	s_mov_b32 m0, s33
	s_add_u32 s14, s14, s29
	s_addc_u32 s15, s15, 0
	global_load_lds_dwordx4 v143, s[18:19]
	global_load_lds_dwordx4 v143, s[18:19] offset:2048
	s_add_u32 m0, m0, 0x1000
	s_add_u32 s18, s18, 0x1000
	s_addc_u32 s19, s19, 0
	global_load_lds_dwordx4 v143, s[18:19]
	global_load_lds_dwordx4 v143, s[18:19] offset:2048
	s_add_u32 m0, m0, 0x1000
	s_add_u32 s18, s18, 0x1000
	s_addc_u32 s19, s19, 0
	global_load_lds_dwordx4 v143, s[18:19]
	global_load_lds_dwordx4 v143, s[18:19] offset:2048
	s_add_u32 m0, m0, 0x1000
	s_add_u32 s18, s18, 0x1000
	s_addc_u32 s19, s19, 0
	global_load_lds_dwordx4 v143, s[18:19]
	global_load_lds_dwordx4 v143, s[18:19] offset:2048
	s_add_u32 s12, s12, s31
	s_addc_u32 s13, s13, 0
	s_add_u32 s16, s16, s31
	s_addc_u32 s17, s17, 0
	s_waitcnt lgkmcnt(0)
	s_lshl_b32 s36, s36, 7
	s_add_u32 s20, s20, s36
	s_addc_u32 s21, s21, 0
	s_lshl_b32 s37, s35, 7
	s_add_u32 s4, s4, s37
	s_addc_u32 s5, s5, 0
	global_load_dwordx4 v[128:131], v142, s[4:5] nt
	global_load_dwordx4 v[132:135], v142, s[4:5] offset:16 nt
	global_load_dword v136, v141, s[12:13] nt
	global_load_dword v137, v141, s[16:17] nt
	global_load_dwordx4 v[64:67], v138, s[14:15] nt
	global_load_dwordx4 v[68:71], v138, s[14:15] offset:256 nt
	global_load_dwordx4 v[72:75], v138, s[14:15] offset:512 nt
	global_load_dwordx4 v[76:79], v138, s[14:15] offset:768 nt
	global_load_dwordx4 v[80:83], v138, s[14:15] offset:1024 nt
	global_load_dwordx4 v[84:87], v138, s[14:15] offset:1280 nt
	global_load_dwordx4 v[88:91], v138, s[14:15] offset:1536 nt
	global_load_dwordx4 v[92:95], v138, s[14:15] offset:1792 nt
	global_load_dwordx4 v[96:99], v138, s[14:15] offset:2048 nt
	global_load_dwordx4 v[100:103], v138, s[14:15] offset:2304 nt
	global_load_dwordx4 v[104:107], v138, s[14:15] offset:2560 nt
	global_load_dwordx4 v[108:111], v138, s[14:15] offset:2816 nt
	global_load_dwordx4 v[112:115], v138, s[14:15] offset:3072 nt
	global_load_dwordx4 v[116:119], v138, s[14:15] offset:3328 nt
	global_load_dwordx4 v[120:123], v138, s[14:15] offset:3584 nt
	global_load_dwordx4 v[124:127], v138, s[14:15] offset:3840 nt
	v_add_u32_e32 v142, s34, v141
	v_lshl_add_u32 v143, v139, 6, s34
	s_waitcnt vmcnt(18)
	s_barrier
	v_cvt_f32_f16_e32 v144, v128
	v_cvt_f32_f16_sdwa v145, v128 dst_sel:DWORD dst_unused:UNUSED_PAD src0_sel:WORD_1
	v_cvt_f32_f16_e32 v146, v129
	v_cvt_f32_f16_sdwa v147, v129 dst_sel:DWORD dst_unused:UNUSED_PAD src0_sel:WORD_1
	v_cvt_f32_f16_e32 v148, v130
	v_cvt_f32_f16_sdwa v149, v130 dst_sel:DWORD dst_unused:UNUSED_PAD src0_sel:WORD_1
	v_cvt_f32_f16_e32 v150, v131
	v_cvt_f32_f16_sdwa v151, v131 dst_sel:DWORD dst_unused:UNUSED_PAD src0_sel:WORD_1
	v_cvt_f32_f16_e32 v152, v132
	v_cvt_f32_f16_sdwa v153, v132 dst_sel:DWORD dst_unused:UNUSED_PAD src0_sel:WORD_1
	v_cvt_f32_f16_e32 v154, v133
	v_cvt_f32_f16_sdwa v155, v133 dst_sel:DWORD dst_unused:UNUSED_PAD src0_sel:WORD_1
	v_cvt_f32_f16_e32 v156, v134
	v_cvt_f32_f16_sdwa v157, v134 dst_sel:DWORD dst_unused:UNUSED_PAD src0_sel:WORD_1
	v_cvt_f32_f16_e32 v158, v135
	v_cvt_f32_f16_sdwa v159, v135 dst_sel:DWORD dst_unused:UNUSED_PAD src0_sel:WORD_1
	v_max_f32_e32 v144, 0, v144
	v_max_f32_e32 v145, 0, v145
	v_max_f32_e32 v146, 0, v146
	v_max_f32_e32 v147, 0, v147
	v_max_f32_e32 v148, 0, v148
	v_max_f32_e32 v149, 0, v149
	v_max_f32_e32 v150, 0, v150
	v_max_f32_e32 v151, 0, v151
	v_max_f32_e32 v152, 0, v152
	v_max_f32_e32 v153, 0, v153
	v_max_f32_e32 v154, 0, v154
	v_max_f32_e32 v155, 0, v155
	v_max_f32_e32 v156, 0, v156
	v_max_f32_e32 v157, 0, v157
	v_max_f32_e32 v158, 0, v158
	v_max_f32_e32 v159, 0, v159
	v_pk_mul_f32 v[160:161], v[144:145], v[0:1] op_sel_hi:[0,1]
	v_pk_mul_f32 v[162:163], v[144:145], v[2:3] op_sel_hi:[0,1]
	v_pk_mul_f32 v[164:165], v[144:145], v[4:5] op_sel:[1,0]
	v_pk_mul_f32 v[166:167], v[144:145], v[6:7] op_sel:[1,0]
	v_pk_fma_f32 v[160:161], v[146:147], v[8:9], v[160:161] op_sel_hi:[0,1,1]
	v_pk_fma_f32 v[162:163], v[146:147], v[10:11], v[162:163] op_sel_hi:[0,1,1]
	v_pk_fma_f32 v[164:165], v[146:147], v[12:13], v[164:165] op_sel:[1,0,0]
	v_pk_fma_f32 v[166:167], v[146:147], v[14:15], v[166:167] op_sel:[1,0,0]
	v_pk_fma_f32 v[160:161], v[148:149], v[16:17], v[160:161] op_sel_hi:[0,1,1]
	v_pk_fma_f32 v[162:163], v[148:149], v[18:19], v[162:163] op_sel_hi:[0,1,1]
	v_pk_fma_f32 v[164:165], v[148:149], v[20:21], v[164:165] op_sel:[1,0,0]
	v_pk_fma_f32 v[166:167], v[148:149], v[22:23], v[166:167] op_sel:[1,0,0]
	v_pk_fma_f32 v[160:161], v[150:151], v[24:25], v[160:161] op_sel_hi:[0,1,1]
	v_pk_fma_f32 v[162:163], v[150:151], v[26:27], v[162:163] op_sel_hi:[0,1,1]
	v_pk_fma_f32 v[164:165], v[150:151], v[28:29], v[164:165] op_sel:[1,0,0]
	v_pk_fma_f32 v[166:167], v[150:151], v[30:31], v[166:167] op_sel:[1,0,0]
	v_pk_fma_f32 v[160:161], v[152:153], v[32:33], v[160:161] op_sel_hi:[0,1,1]
	v_pk_fma_f32 v[162:163], v[152:153], v[34:35], v[162:163] op_sel_hi:[0,1,1]
	v_pk_fma_f32 v[164:165], v[152:153], v[36:37], v[164:165] op_sel:[1,0,0]
	v_pk_fma_f32 v[166:167], v[152:153], v[38:39], v[166:167] op_sel:[1,0,0]
	v_pk_fma_f32 v[160:161], v[154:155], v[40:41], v[160:161] op_sel_hi:[0,1,1]
	v_pk_fma_f32 v[162:163], v[154:155], v[42:43], v[162:163] op_sel_hi:[0,1,1]
	v_pk_fma_f32 v[164:165], v[154:155], v[44:45], v[164:165] op_sel:[1,0,0]
	v_pk_fma_f32 v[166:167], v[154:155], v[46:47], v[166:167] op_sel:[1,0,0]
	v_pk_fma_f32 v[160:161], v[156:157], v[48:49], v[160:161] op_sel_hi:[0,1,1]
	v_pk_fma_f32 v[162:163], v[156:157], v[50:51], v[162:163] op_sel_hi:[0,1,1]
	v_pk_fma_f32 v[164:165], v[156:157], v[52:53], v[164:165] op_sel:[1,0,0]
	v_pk_fma_f32 v[166:167], v[156:157], v[54:55], v[166:167] op_sel:[1,0,0]
	v_pk_fma_f32 v[160:161], v[158:159], v[56:57], v[160:161] op_sel_hi:[0,1,1]
	v_pk_fma_f32 v[162:163], v[158:159], v[58:59], v[162:163] op_sel_hi:[0,1,1]
	v_pk_fma_f32 v[164:165], v[158:159], v[60:61], v[164:165] op_sel:[1,0,0]
	v_pk_fma_f32 v[166:167], v[158:159], v[62:63], v[166:167] op_sel:[1,0,0]
	v_pk_add_f32 v[160:161], v[160:161], v[164:165]
	v_pk_add_f32 v[162:163], v[162:163], v[166:167]
	s_nop 1
	v_permlane16_swap_b32_e32 v160, v161
	v_permlane16_swap_b32_e32 v162, v163
	v_add_f32_e32 v160, v160, v161
	v_add_f32_e32 v162, v162, v163
	s_nop 1
	v_permlane32_swap_b32_e32 v160, v162
	v_add_f32_e32 v160, v160, v162
	s_waitcnt vmcnt(17)
	v_add_f32_e32 v160, v160, v136
	v_max_f32_e32 v160, 0, v160
	ds_write_b32 v142, v160
	ds_read_b128 v[144:147], v143
	ds_read_b128 v[148:151], v143 offset:16
	ds_read_b128 v[152:155], v143 offset:32
	ds_read_b128 v[156:159], v143 offset:48
	ds_read_b128 v[0:3], v138
	ds_read_b128 v[4:7], v138 offset:256
	ds_read_b128 v[8:11], v138 offset:512
	ds_read_b128 v[12:15], v138 offset:768
	ds_read_b128 v[16:19], v138 offset:1024
	ds_read_b128 v[20:23], v138 offset:1280
	ds_read_b128 v[24:27], v138 offset:1536
	ds_read_b128 v[28:31], v138 offset:1792
	s_waitcnt lgkmcnt(8)
	s_waitcnt vmcnt(12)
	v_pk_mul_f32 v[160:161], v[144:145], v[64:65] op_sel_hi:[0,1]
	v_pk_mul_f32 v[162:163], v[144:145], v[66:67] op_sel_hi:[0,1]
	v_pk_mul_f32 v[164:165], v[144:145], v[68:69] op_sel:[1,0]
	v_pk_mul_f32 v[166:167], v[144:145], v[70:71] op_sel:[1,0]
	v_pk_fma_f32 v[160:161], v[146:147], v[72:73], v[160:161] op_sel_hi:[0,1,1]
	v_pk_fma_f32 v[162:163], v[146:147], v[74:75], v[162:163] op_sel_hi:[0,1,1]
	v_pk_fma_f32 v[164:165], v[146:147], v[76:77], v[164:165] op_sel:[1,0,0]
	v_pk_fma_f32 v[166:167], v[146:147], v[78:79], v[166:167] op_sel:[1,0,0]
	ds_read_b128 v[32:35], v138 offset:2048
	ds_read_b128 v[36:39], v138 offset:2304
	ds_read_b128 v[40:43], v138 offset:2560
	ds_read_b128 v[44:47], v138 offset:2816
	s_waitcnt vmcnt(8)
	v_pk_fma_f32 v[160:161], v[148:149], v[80:81], v[160:161] op_sel_hi:[0,1,1]
	v_pk_fma_f32 v[162:163], v[148:149], v[82:83], v[162:163] op_sel_hi:[0,1,1]
	v_pk_fma_f32 v[164:165], v[148:149], v[84:85], v[164:165] op_sel:[1,0,0]
	v_pk_fma_f32 v[166:167], v[148:149], v[86:87], v[166:167] op_sel:[1,0,0]
	v_pk_fma_f32 v[160:161], v[150:151], v[88:89], v[160:161] op_sel_hi:[0,1,1]
	v_pk_fma_f32 v[162:163], v[150:151], v[90:91], v[162:163] op_sel_hi:[0,1,1]
	v_pk_fma_f32 v[164:165], v[150:151], v[92:93], v[164:165] op_sel:[1,0,0]
	v_pk_fma_f32 v[166:167], v[150:151], v[94:95], v[166:167] op_sel:[1,0,0]
	s_waitcnt lgkmcnt(4)
	ds_read_b128 v[48:51], v138 offset:3072
	ds_read_b128 v[52:55], v138 offset:3328
	ds_read_b128 v[56:59], v138 offset:3584
	ds_read_b128 v[60:63], v138 offset:3840
	s_waitcnt vmcnt(4)
	v_pk_fma_f32 v[160:161], v[152:153], v[96:97], v[160:161] op_sel_hi:[0,1,1]
	v_pk_fma_f32 v[162:163], v[152:153], v[98:99], v[162:163] op_sel_hi:[0,1,1]
	v_pk_fma_f32 v[164:165], v[152:153], v[100:101], v[164:165] op_sel:[1,0,0]
	v_pk_fma_f32 v[166:167], v[152:153], v[102:103], v[166:167] op_sel:[1,0,0]
	v_pk_fma_f32 v[160:161], v[154:155], v[104:105], v[160:161] op_sel_hi:[0,1,1]
	v_pk_fma_f32 v[162:163], v[154:155], v[106:107], v[162:163] op_sel_hi:[0,1,1]
	v_pk_fma_f32 v[164:165], v[154:155], v[108:109], v[164:165] op_sel:[1,0,0]
	v_pk_fma_f32 v[166:167], v[154:155], v[110:111], v[166:167] op_sel:[1,0,0]
	s_waitcnt vmcnt(0)
	v_pk_fma_f32 v[160:161], v[156:157], v[112:113], v[160:161] op_sel_hi:[0,1,1]
	v_pk_fma_f32 v[162:163], v[156:157], v[114:115], v[162:163] op_sel_hi:[0,1,1]
	v_pk_fma_f32 v[164:165], v[156:157], v[116:117], v[164:165] op_sel:[1,0,0]
	v_pk_fma_f32 v[166:167], v[156:157], v[118:119], v[166:167] op_sel:[1,0,0]
	v_pk_fma_f32 v[160:161], v[158:159], v[120:121], v[160:161] op_sel_hi:[0,1,1]
	v_pk_fma_f32 v[162:163], v[158:159], v[122:123], v[162:163] op_sel_hi:[0,1,1]
	v_pk_fma_f32 v[164:165], v[158:159], v[124:125], v[164:165] op_sel:[1,0,0]
	v_pk_fma_f32 v[166:167], v[158:159], v[126:127], v[166:167] op_sel:[1,0,0]
	v_pk_add_f32 v[160:161], v[160:161], v[164:165]
	v_pk_add_f32 v[162:163], v[162:163], v[166:167]
	s_nop 1
	v_permlane16_swap_b32_e32 v160, v161
	v_permlane16_swap_b32_e32 v162, v163
	v_add_f32_e32 v160, v160, v161
	v_add_f32_e32 v162, v162, v163
	s_nop 1
	v_permlane32_swap_b32_e32 v160, v162
	v_add_f32_e32 v160, v160, v162
	v_add_f32_e32 v160, v160, v137
	ds_write_b32 v142, v160
	ds_read_b128 v[144:147], v143
	ds_read_b128 v[148:151], v143 offset:16
	ds_read_b128 v[152:155], v143 offset:32
	ds_read_b128 v[156:159], v143 offset:48
	v_lshlrev_b32_e32 v136, 3, v140
	v_lshl_or_b32 v136, v139, 2, v136
	v_cmp_gt_u32_e32 vcc, 2, v139
	s_waitcnt lgkmcnt(0)
	v_pk_mul_f32 v[160:161], v[144:145], v[0:1] op_sel_hi:[0,1]
	v_pk_mul_f32 v[162:163], v[144:145], v[2:3] op_sel_hi:[0,1]
	v_pk_mul_f32 v[164:165], v[144:145], v[4:5] op_sel:[1,0]
	v_pk_mul_f32 v[166:167], v[144:145], v[6:7] op_sel:[1,0]
	v_pk_fma_f32 v[160:161], v[146:147], v[8:9], v[160:161] op_sel_hi:[0,1,1]
	v_pk_fma_f32 v[162:163], v[146:147], v[10:11], v[162:163] op_sel_hi:[0,1,1]
	v_pk_fma_f32 v[164:165], v[146:147], v[12:13], v[164:165] op_sel:[1,0,0]
	v_pk_fma_f32 v[166:167], v[146:147], v[14:15], v[166:167] op_sel:[1,0,0]
	v_pk_fma_f32 v[160:161], v[148:149], v[16:17], v[160:161] op_sel_hi:[0,1,1]
	v_pk_fma_f32 v[162:163], v[148:149], v[18:19], v[162:163] op_sel_hi:[0,1,1]
	v_pk_fma_f32 v[164:165], v[148:149], v[20:21], v[164:165] op_sel:[1,0,0]
	v_pk_fma_f32 v[166:167], v[148:149], v[22:23], v[166:167] op_sel:[1,0,0]
	v_pk_fma_f32 v[160:161], v[150:151], v[24:25], v[160:161] op_sel_hi:[0,1,1]
	v_pk_fma_f32 v[162:163], v[150:151], v[26:27], v[162:163] op_sel_hi:[0,1,1]
	v_pk_fma_f32 v[164:165], v[150:151], v[28:29], v[164:165] op_sel:[1,0,0]
	v_pk_fma_f32 v[166:167], v[150:151], v[30:31], v[166:167] op_sel:[1,0,0]
	v_pk_fma_f32 v[160:161], v[152:153], v[32:33], v[160:161] op_sel_hi:[0,1,1]
	v_pk_fma_f32 v[162:163], v[152:153], v[34:35], v[162:163] op_sel_hi:[0,1,1]
	v_pk_fma_f32 v[164:165], v[152:153], v[36:37], v[164:165] op_sel:[1,0,0]
	v_pk_fma_f32 v[166:167], v[152:153], v[38:39], v[166:167] op_sel:[1,0,0]
	v_pk_fma_f32 v[160:161], v[154:155], v[40:41], v[160:161] op_sel_hi:[0,1,1]
	v_pk_fma_f32 v[162:163], v[154:155], v[42:43], v[162:163] op_sel_hi:[0,1,1]
	v_pk_fma_f32 v[164:165], v[154:155], v[44:45], v[164:165] op_sel:[1,0,0]
	v_pk_fma_f32 v[166:167], v[154:155], v[46:47], v[166:167] op_sel:[1,0,0]
	v_pk_fma_f32 v[160:161], v[156:157], v[48:49], v[160:161] op_sel_hi:[0,1,1]
	v_pk_fma_f32 v[162:163], v[156:157], v[50:51], v[162:163] op_sel_hi:[0,1,1]
	v_pk_fma_f32 v[164:165], v[156:157], v[52:53], v[164:165] op_sel:[1,0,0]
	v_pk_fma_f32 v[166:167], v[156:157], v[54:55], v[166:167] op_sel:[1,0,0]
	v_pk_fma_f32 v[160:161], v[158:159], v[56:57], v[160:161] op_sel_hi:[0,1,1]
	v_pk_fma_f32 v[162:163], v[158:159], v[58:59], v[162:163] op_sel_hi:[0,1,1]
	v_pk_fma_f32 v[164:165], v[158:159], v[60:61], v[164:165] op_sel:[1,0,0]
	v_pk_fma_f32 v[166:167], v[158:159], v[62:63], v[166:167] op_sel:[1,0,0]
	v_pk_add_f32 v[160:161], v[160:161], v[164:165]
	v_pk_add_f32 v[162:163], v[162:163], v[166:167]
	s_nop 1
	v_permlane16_swap_b32_e32 v160, v162
	v_permlane16_swap_b32_e32 v161, v163
	v_add_f32_e32 v160, v160, v162
	v_add_f32_e32 v161, v161, v163
	v_mov_b32_e32 v144, v160
	v_mov_b32_e32 v145, v161
	s_nop 1
	v_permlane32_swap_b32_e32 v160, v144
	v_permlane32_swap_b32_e32 v161, v145
	v_add_f32_e32 v160, v160, v144
	v_add_f32_e32 v161, v161, v145
	v_cvt_pk_f16_f32 v137, v160, v161
	s_and_saveexec_b64 s[4:5], vcc
	global_atomic_pk_add_f16 v136, v137, s[20:21]
	s_endpgm
	.p2align	8

	.amdhsa_kernel _Z11edge_kernelILi64ELb0EEvPKfS1_PKDF16_PKiS5_S1_S1_S1_S1_S1_PDF16_
		.amdhsa_group_segment_fixed_size 16896
		.amdhsa_private_segment_fixed_size 0
		.amdhsa_kernarg_size 88
		.amdhsa_user_sgpr_count 2
		.amdhsa_user_sgpr_dispatch_ptr 0
		.amdhsa_user_sgpr_queue_ptr 0
		.amdhsa_user_sgpr_kernarg_segment_ptr 1
		.amdhsa_user_sgpr_dispatch_id 0
		.amdhsa_user_sgpr_kernarg_preload_length 0
		.amdhsa_user_sgpr_kernarg_preload_offset 0
		.amdhsa_user_sgpr_private_segment_size 0
		.amdhsa_uses_dynamic_stack 0
		.amdhsa_enable_private_segment 0
		.amdhsa_system_sgpr_workgroup_id_x 1
		.amdhsa_system_sgpr_workgroup_id_y 0
		.amdhsa_system_sgpr_workgroup_id_z 0
		.amdhsa_system_sgpr_workgroup_info 0
		.amdhsa_system_vgpr_workitem_id 0
		.amdhsa_next_free_vgpr 168
		.amdhsa_next_free_sgpr 96
		.amdhsa_accum_offset 168
		.amdhsa_reserve_vcc 1
		.amdhsa_float_round_mode_32 0
		.amdhsa_float_round_mode_16_64 0
		.amdhsa_float_denorm_mode_32 3
		.amdhsa_float_denorm_mode_16_64 3
		.amdhsa_dx10_clamp 1
		.amdhsa_ieee_mode 1
		.amdhsa_fp16_overflow 0
		.amdhsa_tg_split 0
		.amdhsa_exception_fp_ieee_invalid_op 0
		.amdhsa_exception_fp_denorm_src 0
		.amdhsa_exception_fp_ieee_div_zero 0
		.amdhsa_exception_fp_ieee_overflow 0
		.amdhsa_exception_fp_ieee_underflow 0
		.amdhsa_exception_fp_ieee_inexact 0
		.amdhsa_exception_int_div_zero 0
	.end_amdhsa_kernel

amdhsa.kernels:
  - .agpr_count:     8
    .args:
      - .actual_access:  read_only
        .address_space:  global
        .offset:         0
        .size:           8
        .value_kind:     global_buffer
      - .actual_access:  read_only
        .address_space:  global
        .offset:         8
        .size:           8
        .value_kind:     global_buffer
      - .actual_access:  read_only
        .address_space:  global
        .offset:         16
        .size:           8
        .value_kind:     global_buffer
      - .actual_access:  read_only
        .address_space:  global
        .offset:         24
        .size:           8
        .value_kind:     global_buffer
      - .actual_access:  write_only
        .address_space:  global
        .offset:         32
        .size:           8
        .value_kind:     global_buffer
      - .actual_access:  write_only
        .address_space:  global
        .offset:         40
        .size:           8
        .value_kind:     global_buffer
    .group_segment_fixed_size: 4224
    .kernarg_segment_align: 8
    .kernarg_segment_size: 48
    .language:       OpenCL C
    .language_version:
      - 2
      - 0
    .max_flat_workgroup_size: 128
    .name:           _Z11init_kernelPKfS0_S0_S0_PDF16_S1_
    .private_segment_fixed_size: 0
    .sgpr_count:     22
    .sgpr_spill_count: 0
    .symbol:         _Z11init_kernelPKfS0_S0_S0_PDF16_S1_.kd
    .uniform_work_group_size: 1
    .uses_dynamic_stack: false
    .vgpr_count:     52
    .vgpr_spill_count: 0
    .wavefront_size: 64
  - .agpr_count:     8
    .args:
      - .actual_access:  read_only
        .address_space:  global
        .offset:         0
        .size:           8
        .value_kind:     global_buffer
      - .actual_access:  read_only
        .address_space:  global
        .offset:         8
        .size:           8
        .value_kind:     global_buffer
      - .actual_access:  read_only
        .address_space:  global
        .offset:         16
        .size:           8
        .value_kind:     global_buffer
      - .actual_access:  read_only
        .address_space:  global
        .offset:         24
        .size:           8
        .value_kind:     global_buffer
      - .actual_access:  read_only
        .address_space:  global
        .offset:         32
        .size:           8
        .value_kind:     global_buffer
      - .actual_access:  read_only
        .address_space:  global
        .offset:         40
        .size:           8
        .value_kind:     global_buffer
      - .actual_access:  write_only
        .address_space:  global
        .offset:         48
        .size:           8
        .value_kind:     global_buffer
    .group_segment_fixed_size: 4352
    .kernarg_segment_align: 8
    .kernarg_segment_size: 56
    .language:       OpenCL C
    .language_version:
      - 2
      - 0
    .max_flat_workgroup_size: 128
    .name:           _Z12final_kernelPKDF16_S0_PKfS2_S2_S2_Pf
    .private_segment_fixed_size: 0
    .sgpr_count:     26
    .sgpr_spill_count: 0
    .symbol:         _Z12final_kernelPKDF16_S0_PKfS2_S2_S2_Pf.kd
    .uniform_work_group_size: 1
    .uses_dynamic_stack: false
    .vgpr_count:     60
    .vgpr_spill_count: 0
    .wavefront_size: 64
  - .agpr_count:     0
    .args:
      - .actual_access:  read_only
        .address_space:  global
        .offset:         0
        .size:           8
        .value_kind:     global_buffer
      - .actual_access:  read_only
        .address_space:  global
        .offset:         8
        .size:           8
        .value_kind:     global_buffer
      - .actual_access:  read_only
        .address_space:  global
        .offset:         16
        .size:           8
        .value_kind:     global_buffer
      - .actual_access:  read_only
        .address_space:  global
        .offset:         24
        .size:           8
        .value_kind:     global_buffer
      - .actual_access:  read_only
        .address_space:  global
        .offset:         32
        .size:           8
        .value_kind:     global_buffer
      - .actual_access:  read_only
        .address_space:  global
        .offset:         40
        .size:           8
        .value_kind:     global_buffer
      - .actual_access:  read_only
        .address_space:  global
        .offset:         48
        .size:           8
        .value_kind:     global_buffer
      - .actual_access:  read_only
        .address_space:  global
        .offset:         56
        .size:           8
        .value_kind:     global_buffer
      - .actual_access:  read_only
        .address_space:  global
        .offset:         64
        .size:           8
        .value_kind:     global_buffer
      - .actual_access:  read_only
        .address_space:  global
        .offset:         72
        .size:           8
        .value_kind:     global_buffer
      - .address_space:  global
        .offset:         80
        .size:           8
        .value_kind:     global_buffer
    .group_segment_fixed_size: 16896
    .kernarg_segment_align: 8
    .kernarg_segment_size: 88
    .language:       OpenCL C
    .language_version:
      - 2
      - 0
    .max_flat_workgroup_size: 128
    .name:           _Z11edge_kernelILi36ELb1EEvPKfS1_PKDF16_PKiS5_S1_S1_S1_S1_S1_PDF16_
    .private_segment_fixed_size: 0
    .sgpr_count:     23
    .sgpr_spill_count: 0
    .symbol:         _Z11edge_kernelILi36ELb1EEvPKfS1_PKDF16_PKiS5_S1_S1_S1_S1_S1_PDF16_.kd
    .uniform_work_group_size: 1
    .uses_dynamic_stack: false
    .vgpr_count:     168
    .vgpr_spill_count: 0
    .wavefront_size: 64
  - .agpr_count:     0
    .args:
      - .actual_access:  read_only
        .address_space:  global
        .offset:         0
        .size:           8
        .value_kind:     global_buffer
      - .actual_access:  read_only
        .address_space:  global
        .offset:         8
        .size:           8
        .value_kind:     global_buffer
      - .actual_access:  read_only
        .address_space:  global
        .offset:         16
        .size:           8
        .value_kind:     global_buffer
      - .actual_access:  read_only
        .address_space:  global
        .offset:         24
        .size:           8
        .value_kind:     global_buffer
      - .actual_access:  read_only
        .address_space:  global
        .offset:         32
        .size:           8
        .value_kind:     global_buffer
      - .actual_access:  read_only
        .address_space:  global
        .offset:         40
        .size:           8
        .value_kind:     global_buffer
      - .actual_access:  read_only
        .address_space:  global
        .offset:         48
        .size:           8
        .value_kind:     global_buffer
      - .actual_access:  read_only
        .address_space:  global
        .offset:         56
        .size:           8
        .value_kind:     global_buffer
      - .actual_access:  read_only
        .address_space:  global
        .offset:         64
        .size:           8
        .value_kind:     global_buffer
      - .actual_access:  read_only
        .address_space:  global
        .offset:         72
        .size:           8
        .value_kind:     global_buffer
      - .address_space:  global
        .offset:         80
        .size:           8
        .value_kind:     global_buffer
    .group_segment_fixed_size: 16896
    .kernarg_segment_align: 8
    .kernarg_segment_size: 88
    .language:       OpenCL C
    .language_version:
      - 2
      - 0
    .max_flat_workgroup_size: 128
    .name:           _Z11edge_kernelILi64ELb0EEvPKfS1_PKDF16_PKiS5_S1_S1_S1_S1_S1_PDF16_
    .private_segment_fixed_size: 0
    .sgpr_count:     26
    .sgpr_spill_count: 0
    .symbol:         _Z11edge_kernelILi64ELb0EEvPKfS1_PKDF16_PKiS5_S1_S1_S1_S1_S1_PDF16_.kd
    .uniform_work_group_size: 1
    .uses_dynamic_stack: false
    .vgpr_count:     168
    .vgpr_spill_count: 0
    .wavefront_size: 64
